# speedup vs baseline: 1.0311x; 1.0072x over previous
_Z8k2_fusedPKDF16_PKDv8_DF16_PKfS5_S5_PfPiS6_:
	s_lshl_b32 s3, s2, 2
	s_ashr_i32 s16, s2, 4
	s_and_b32 s12, s3, 48
	s_lshl_b32 s2, s2, 4
	s_and_b32 s13, s2, 48
	s_add_i32 s2, s12, -2
	v_mul_u32_u24_e32 v1, 0x334, v0
	s_movk_i32 s15, 0xffec
	s_add_i32 s3, s13, -2
	v_lshrrev_b32_e32 v84, 2, v0
	v_mul_i32_i24_sdwa v2, v1, s15 dst_sel:DWORD dst_unused:UNUSED_PAD src0_sel:WORD_1 src1_sel:DWORD
	v_add_u32_sdwa v48, s2, v1 dst_sel:DWORD dst_unused:UNUSED_PAD src0_sel:DWORD src1_sel:WORD_1
	s_load_dwordx8 s[4:11], s[0:1], 0x0
	s_load_dwordx4 s[32:35], s[0:1], 0x20
	s_load_dwordx2 s[36:37], s[0:1], 0x38
	v_add3_u32 v49, s3, v84, v2
	v_max_i32_e32 v1, 0, v48
	s_lshl_b32 s14, s16, 12
	v_med3_i32 v2, v49, 0, 63
	v_lshlrev_b32_e32 v1, 6, v1
	v_or3_b32 v1, v1, v2, s14
	v_lshlrev_b32_e32 v2, 5, v1
	v_ashrrev_i32_e32 v3, 31, v2
	v_lshlrev_b32_e32 v85, 4, v0
	s_waitcnt lgkmcnt(0)
	v_lshl_add_u64 v[2:3], v[2:3], 1, s[4:5]
	v_and_b32_e32 v46, 48, v85
	v_mov_b32_e32 v47, 0
	v_or_b32_e32 v54, 0x200, v0
	v_lshl_add_u64 v[2:3], v[2:3], 0, v[46:47]
	v_mul_u32_u24_e32 v1, 0x334, v54
	global_load_dwordx4 v[18:21], v[2:3], off
	v_lshrrev_b32_e32 v86, 2, v54
	v_mul_i32_i24_sdwa v2, v1, s15 dst_sel:DWORD dst_unused:UNUSED_PAD src0_sel:WORD_1 src1_sel:DWORD
	v_add_u32_sdwa v50, s2, v1 dst_sel:DWORD dst_unused:UNUSED_PAD src0_sel:DWORD src1_sel:WORD_1
	v_add3_u32 v51, s3, v86, v2
	v_min_u32_e32 v1, 63, v50
	v_med3_i32 v2, v51, 0, 63
	v_lshlrev_b32_e32 v1, 6, v1
	v_or3_b32 v1, v1, v2, s14
	v_lshlrev_b32_e32 v2, 5, v1
	v_or_b32_e32 v58, 0x400, v0
	v_ashrrev_i32_e32 v3, 31, v2
	v_lshlrev_b32_e32 v87, 4, v54
	v_mul_u32_u24_e32 v1, 0x667, v58
	v_lshl_add_u64 v[2:3], v[2:3], 1, s[4:5]
	v_and_b32_e32 v4, 48, v87
	v_mov_b32_e32 v5, v47
	v_lshrrev_b32_e32 v1, 17, v1
	v_lshl_add_u64 v[2:3], v[2:3], 0, v[4:5]
	v_mul_i32_i24_e32 v4, 0xffffffec, v1
	v_add_u32_e32 v52, s2, v1
	v_lshrrev_b32_e32 v88, 2, v58
	v_add3_u32 v53, s3, v88, v4
	v_min_u32_e32 v1, 63, v52
	v_med3_i32 v4, v53, 0, 63
	v_lshlrev_b32_e32 v1, 6, v1
	v_or3_b32 v1, v1, v4, s14
	v_lshlrev_b32_e32 v4, 5, v1
	v_ashrrev_i32_e32 v5, 31, v4
	v_or_b32_e32 v89, 0x600, v0
	v_lshl_add_u64 v[4:5], v[4:5], 1, s[4:5]
	v_min_u32_e32 v1, 0x63f, v89
	v_lshl_add_u64 v[4:5], v[4:5], 0, v[46:47]
	global_load_dwordx4 v[22:25], v[2:3], off
	global_load_dwordx4 v[26:29], v[4:5], off
	v_lshrrev_b32_e32 v2, 2, v1
	v_add_u32_e32 v2, s3, v2
	s_add_i32 s15, s12, 17
	v_add_u32_e32 v55, 0xfffffe84, v2
	s_min_u32 s2, s15, 63
	v_min_u32_e32 v2, 63, v55
	v_lshl_or_b32 v2, s2, 6, v2
	v_or_b32_e32 v2, s14, v2
	v_lshlrev_b32_e32 v2, 5, v2
	v_ashrrev_i32_e32 v3, 31, v2
	v_lshlrev_b32_e32 v1, 4, v1
	v_lshl_add_u64 v[2:3], v[2:3], 1, s[4:5]
	v_and_b32_e32 v4, 48, v1
	v_mov_b32_e32 v5, v47
	v_min_u32_e32 v1, 0x47f, v58
	v_lshrrev_b32_e32 v164, 1, v0
	v_lshl_add_u64 v[2:3], v[2:3], 0, v[4:5]
	v_lshlrev_b32_e32 v90, 4, v1
	v_and_b32_e32 v162, 16, v164
	global_load_dwordx4 v[30:33], v[2:3], off
	global_load_dwordx4 v[34:37], v85, s[6:7]
	global_load_dwordx4 v[38:41], v87, s[6:7]
	global_load_dwordx4 v[42:45], v90, s[6:7]
	s_nop 0
	global_load_dwordx4 v[2:5], v162, s[8:9]
	global_load_dwordx4 v[6:9], v162, s[8:9] offset:32
	global_load_dwordx4 v[10:13], v162, s[8:9] offset:64
	global_load_dwordx4 v[14:17], v162, s[8:9] offset:96
	v_or_b32_e32 v48, v48, v49
	v_cmp_gt_u32_e32 vcc, 64, v48
	v_or_b32_e32 v48, v50, v51
	v_cmp_gt_u32_e64 s[2:3], 64, v48
	v_or_b32_e32 v48, v52, v53
	v_and_b32_e32 v1, 63, v0
	v_and_b32_e32 v165, 31, v0
	v_cmp_gt_u32_e64 s[4:5], 64, v48
	v_or_b32_e32 v48, s15, v55
	v_lshrrev_b32_e32 v163, 6, v0
	v_cmp_gt_u32_e64 s[6:7], 64, v48
	s_lshr_b32 s8, s12, 1
	s_lshr_b32 s26, s13, 1
	v_add_u32_e32 v48, s8, v163
	v_bfe_u32 v49, v0, 1, 3
	v_add_u32_e32 v49, s26, v49
	v_lshlrev_b32_e32 v48, 10, v48
	v_lshl_or_b32 v48, v49, 5, v48
	v_bfe_u32 v49, v0, 5, 1
	v_lshl_or_b32 v48, v49, 2, v48
	v_bfe_u32 v49, v0, 4, 1
	v_lshl_or_b32 v48, v49, 1, v48
	v_and_b32_e32 v49, 1, v0
	v_or_b32_e32 v48, v48, v49
	v_mul_u32_u24_e32 v59, 40, v48
	global_load_dwordx4 v[66:69], v59, s[10:11]
	global_load_dwordx4 v[50:53], v59, s[10:11] offset:16
	global_load_dwordx2 v[156:157], v59, s[10:11] offset:32
	global_load_dwordx4 v[70:73], v59, s[10:11] offset:320
	global_load_dwordx4 v[54:57], v59, s[10:11] offset:336
	global_load_dwordx2 v[154:155], v59, s[10:11] offset:352
	global_load_dwordx4 v[74:77], v59, s[10:11] offset:640
	global_load_dwordx4 v[58:61], v59, s[10:11] offset:656
	global_load_dwordx2 v[160:161], v59, s[10:11] offset:672
	global_load_dwordx4 v[78:81], v59, s[10:11] offset:960
	global_load_dwordx4 v[62:65], v59, s[10:11] offset:976
	global_load_dwordx2 v[158:159], v59, s[10:11] offset:992
	s_movk_i32 s8, 0x50
	s_waitcnt vmcnt(22)
	v_cndmask_b32_e32 v19, 0, v19, vcc
	v_cndmask_b32_e32 v18, 0, v18, vcc
	v_cndmask_b32_e32 v21, 0, v21, vcc
	v_cndmask_b32_e32 v20, 0, v20, vcc
	v_mad_u32_u24 v47, v84, s8, v46
	ds_write_b128 v47, v[18:21]
	s_waitcnt vmcnt(21)
	v_cndmask_b32_e64 v19, 0, v23, s[2:3]
	v_cndmask_b32_e64 v18, 0, v22, s[2:3]
	v_cndmask_b32_e64 v21, 0, v25, s[2:3]
	v_cndmask_b32_e64 v20, 0, v24, s[2:3]
	v_mad_u32_u24 v22, v86, s8, v46
	ds_write_b128 v22, v[18:21]
	s_waitcnt vmcnt(20)
	v_cndmask_b32_e64 v19, 0, v27, s[4:5]
	v_cndmask_b32_e64 v18, 0, v26, s[4:5]
	v_cndmask_b32_e64 v21, 0, v29, s[4:5]
	v_cndmask_b32_e64 v20, 0, v28, s[4:5]
	v_mad_u32_u24 v22, v88, s8, v46
	ds_write_b128 v22, v[18:21]
	v_lshrrev_b32_e32 v22, 2, v89
	s_waitcnt vmcnt(19)
	v_cndmask_b32_e64 v19, 0, v31, s[6:7]
	v_cndmask_b32_e64 v18, 0, v30, s[6:7]
	v_cndmask_b32_e64 v21, 0, v33, s[6:7]
	v_cndmask_b32_e64 v20, 0, v32, s[6:7]
	v_mad_u32_u24 v22, v22, s8, v46
	ds_write_b128 v22, v[18:21]
	s_waitcnt vmcnt(18)
	ds_write_b128 v85, v[34:37] offset:57920
	s_waitcnt vmcnt(17)
	ds_write_b128 v87, v[38:41] offset:57920
	s_waitcnt vmcnt(16)
	ds_write_b128 v90, v[42:45] offset:57920
	v_lshlrev_b32_e32 v197, 4, v1
	v_lshl_or_b32 v166, v163, 5, v165
	v_mul_u32_u24_e32 v20, 0xe39, v166
	v_lshrrev_b32_e32 v168, 16, v20
	s_movk_i32 s4, 0xffee
	v_mad_i32_i24 v169, v168, s4, v166
	v_min_u32_e32 v21, 0x43, v166
	v_mad_u32_u24 v20, v168, 20, v169
	v_or_b32_e32 v165, 0x100, v21
	s_movk_i32 s2, 0xc0
	v_mul_lo_u32 v20, v20, s8
	v_mul_u32_u24_e32 v21, 0xe39, v165
	v_cmp_gt_u32_e32 vcc, s2, v0
	s_movk_i32 s2, 0xbf
	v_lshrrev_b32_e32 v167, 16, v21
	v_cmp_lt_u32_e64 s[2:3], s2, v0
	v_add_u32_e32 v171, v20, v162
	v_mad_i32_i24 v170, v167, s4, v165
	v_mad_u32_u24 v20, v167, 20, v170
	s_movk_i32 s26, 0x50
	v_mad_u32_u24 v208, v20, s26, v162
	v_add_u32_e32 v198, 0xe240, v197
	s_waitcnt lgkmcnt(0)
	s_barrier
	s_and_saveexec_b64 s[6:7], s[2:3]
	s_xor_b64 s[2:3], exec, s[6:7]
	s_cbranch_execz .LBB1_2
	ds_read_b128 v[172:175], v171
	ds_read_b128 v[150:153], v197 offset:57920
	ds_read_b128 v[176:179], v171 offset:32
	ds_read_b128 v[146:149], v197 offset:58944
	ds_read_b128 v[180:183], v171 offset:80
	ds_read_b128 v[142:145], v197 offset:59968
	ds_read_b128 v[184:187], v171 offset:112
	ds_read_b128 v[138:141], v197 offset:60992
	ds_read_b128 v[188:191], v171 offset:160
	ds_read_b128 v[134:137], v197 offset:62016
	ds_read_b128 v[192:195], v171 offset:192
	ds_read_b128 v[130:133], v197 offset:63040
	s_waitcnt vmcnt(12) lgkmcnt(10)
	v_mfma_f32_32x32x16_f16 v[18:33], v[150:153], v[172:175], v[2:17]
	ds_read_b128 v[172:175], v171 offset:1600
	ds_read_b128 v[126:129], v197 offset:64064
	s_waitcnt lgkmcnt(10)
	v_mfma_f32_32x32x16_f16 v[18:33], v[146:149], v[176:179], v[18:33]
	ds_read_b128 v[176:179], v171 offset:1632
	ds_read_b128 v[122:125], v197 offset:65088
	s_waitcnt lgkmcnt(10)
	v_mfma_f32_32x32x16_f16 v[18:33], v[142:145], v[180:183], v[18:33]
	ds_read_b128 v[180:183], v171 offset:1680
	ds_read_b128 v[118:121], v198 offset:8192
	s_waitcnt lgkmcnt(10)
	v_mfma_f32_32x32x16_f16 v[18:33], v[138:141], v[184:187], v[18:33]
	ds_read_b128 v[184:187], v171 offset:1712
	ds_read_b128 v[114:117], v198 offset:9216
	s_waitcnt lgkmcnt(10)
	v_mfma_f32_32x32x16_f16 v[18:33], v[134:137], v[188:191], v[18:33]
	ds_read_b128 v[188:191], v171 offset:1760
	ds_read_b128 v[110:113], v198 offset:10240
	s_waitcnt lgkmcnt(10)
	v_mfma_f32_32x32x16_f16 v[18:33], v[130:133], v[192:195], v[18:33]
	ds_read_b128 v[192:195], v171 offset:1792
	ds_read_b128 v[106:109], v198 offset:11264
	s_waitcnt lgkmcnt(10)
	v_mfma_f32_32x32x16_f16 v[18:33], v[126:129], v[172:175], v[18:33]
	ds_read_b128 v[172:175], v171 offset:3200
	ds_read_b128 v[102:105], v198 offset:12288
	s_waitcnt lgkmcnt(10)
	v_mfma_f32_32x32x16_f16 v[18:33], v[122:125], v[176:179], v[18:33]
	ds_read_b128 v[176:179], v171 offset:3232
	ds_read_b128 v[98:101], v198 offset:13312
	s_waitcnt lgkmcnt(10)
	v_mfma_f32_32x32x16_f16 v[18:33], v[118:121], v[180:183], v[18:33]
	ds_read_b128 v[180:183], v171 offset:3280
	ds_read_b128 v[94:97], v198 offset:14336
	s_waitcnt lgkmcnt(10)
	v_mfma_f32_32x32x16_f16 v[18:33], v[114:117], v[184:187], v[18:33]
	ds_read_b128 v[184:187], v171 offset:3312
	ds_read_b128 v[90:93], v198 offset:15360
	s_waitcnt lgkmcnt(10)
	v_mfma_f32_32x32x16_f16 v[18:33], v[110:113], v[188:191], v[18:33]
	ds_read_b128 v[188:191], v171 offset:3360
	ds_read_b128 v[86:89], v198 offset:16384
	s_waitcnt lgkmcnt(10)
	v_mfma_f32_32x32x16_f16 v[18:33], v[106:109], v[192:195], v[18:33]
	ds_read_b128 v[192:195], v171 offset:3392
	ds_read_b128 v[82:85], v198 offset:17408
	s_waitcnt lgkmcnt(10)
	v_mfma_f32_32x32x16_f16 v[18:33], v[102:105], v[172:175], v[18:33]
	s_waitcnt lgkmcnt(8)
	v_mfma_f32_32x32x16_f16 v[18:33], v[98:101], v[176:179], v[18:33]
	s_waitcnt lgkmcnt(6)
	v_mfma_f32_32x32x16_f16 v[18:33], v[94:97], v[180:183], v[18:33]
	s_waitcnt lgkmcnt(4)
	v_mfma_f32_32x32x16_f16 v[18:33], v[90:93], v[184:187], v[18:33]
	s_waitcnt lgkmcnt(2)
	v_mfma_f32_32x32x16_f16 v[18:33], v[86:89], v[188:191], v[18:33]
	s_waitcnt lgkmcnt(0)
	v_mfma_f32_32x32x16_f16 v[18:33], v[82:85], v[192:195], v[18:33]
.LBB1_2:
	s_or_saveexec_b64 s[2:3], s[2:3]
	s_xor_b64 exec, exec, s[2:3]
	s_cbranch_execz .LBB1_4
	ds_read_b128 v[172:175], v171
	ds_read_b128 v[150:153], v197 offset:57920
	ds_read_b128 v[176:179], v171 offset:32
	ds_read_b128 v[146:149], v197 offset:58944
	ds_read_b128 v[180:183], v171 offset:80
	ds_read_b128 v[142:145], v197 offset:59968
	ds_read_b128 v[184:187], v171 offset:112
	ds_read_b128 v[138:141], v197 offset:60992
	ds_read_b128 v[188:191], v171 offset:160
	ds_read_b128 v[134:137], v197 offset:62016
	ds_read_b128 v[192:195], v171 offset:192
	ds_read_b128 v[130:133], v197 offset:63040
	s_waitcnt vmcnt(12) lgkmcnt(10)
	v_mfma_f32_32x32x16_f16 v[18:33], v[150:153], v[172:175], v[2:17]
	ds_read_b128 v[172:175], v171 offset:1600
	ds_read_b128 v[126:129], v197 offset:64064
	s_waitcnt lgkmcnt(10)
	v_mfma_f32_32x32x16_f16 v[18:33], v[146:149], v[176:179], v[18:33]
	ds_read_b128 v[176:179], v171 offset:1632
	ds_read_b128 v[122:125], v197 offset:65088
	s_waitcnt lgkmcnt(10)
	v_mfma_f32_32x32x16_f16 v[18:33], v[142:145], v[180:183], v[18:33]
	ds_read_b128 v[180:183], v171 offset:1680
	ds_read_b128 v[118:121], v198 offset:8192
	s_waitcnt lgkmcnt(10)
	v_mfma_f32_32x32x16_f16 v[18:33], v[138:141], v[184:187], v[18:33]
	ds_read_b128 v[184:187], v171 offset:1712
	ds_read_b128 v[114:117], v198 offset:9216
	s_waitcnt lgkmcnt(10)
	v_mfma_f32_32x32x16_f16 v[18:33], v[134:137], v[188:191], v[18:33]
	ds_read_b128 v[188:191], v171 offset:1760
	ds_read_b128 v[110:113], v198 offset:10240
	s_waitcnt lgkmcnt(10)
	v_mfma_f32_32x32x16_f16 v[18:33], v[130:133], v[192:195], v[18:33]
	ds_read_b128 v[192:195], v171 offset:1792
	ds_read_b128 v[106:109], v198 offset:11264
	s_waitcnt lgkmcnt(10)
	v_mfma_f32_32x32x16_f16 v[18:33], v[126:129], v[172:175], v[18:33]
	ds_read_b128 v[172:175], v171 offset:3200
	ds_read_b128 v[102:105], v198 offset:12288
	s_waitcnt lgkmcnt(10)
	v_mfma_f32_32x32x16_f16 v[18:33], v[122:125], v[176:179], v[18:33]
	ds_read_b128 v[176:179], v171 offset:3232
	ds_read_b128 v[98:101], v198 offset:13312
	s_waitcnt lgkmcnt(10)
	v_mfma_f32_32x32x16_f16 v[18:33], v[118:121], v[180:183], v[18:33]
	ds_read_b128 v[180:183], v171 offset:3280
	ds_read_b128 v[94:97], v198 offset:14336
	s_waitcnt lgkmcnt(10)
	v_mfma_f32_32x32x16_f16 v[18:33], v[114:117], v[184:187], v[18:33]
	ds_read_b128 v[184:187], v171 offset:3312
	ds_read_b128 v[90:93], v198 offset:15360
	s_waitcnt lgkmcnt(10)
	v_mfma_f32_32x32x16_f16 v[18:33], v[110:113], v[188:191], v[18:33]
	ds_read_b128 v[188:191], v171 offset:3360
	ds_read_b128 v[86:89], v198 offset:16384
	s_waitcnt lgkmcnt(10)
	v_mfma_f32_32x32x16_f16 v[18:33], v[106:109], v[192:195], v[18:33]
	ds_read_b128 v[192:195], v171 offset:3392
	ds_read_b128 v[82:85], v198 offset:17408
	s_waitcnt lgkmcnt(10)
	v_mfma_f32_32x32x16_f16 v[18:33], v[102:105], v[172:175], v[18:33]
	ds_read_b128 v[172:175], v208
	s_waitcnt lgkmcnt(9)
	v_mfma_f32_32x32x16_f16 v[18:33], v[98:101], v[176:179], v[18:33]
	ds_read_b128 v[176:179], v208 offset:32
	s_waitcnt lgkmcnt(8)
	v_mfma_f32_32x32x16_f16 v[18:33], v[94:97], v[180:183], v[18:33]
	ds_read_b128 v[180:183], v208 offset:80
	s_waitcnt lgkmcnt(7)
	v_mfma_f32_32x32x16_f16 v[18:33], v[90:93], v[184:187], v[18:33]
	ds_read_b128 v[184:187], v208 offset:112
	s_waitcnt lgkmcnt(6)
	v_mfma_f32_32x32x16_f16 v[18:33], v[86:89], v[188:191], v[18:33]
	ds_read_b128 v[188:191], v208 offset:160
	s_waitcnt lgkmcnt(5)
	v_mfma_f32_32x32x16_f16 v[18:33], v[82:85], v[192:195], v[18:33]
	ds_read_b128 v[192:195], v208 offset:192
	s_waitcnt lgkmcnt(5)
	v_mfma_f32_32x32x16_f16 v[34:49], v[150:153], v[172:175], v[2:17]
	ds_read_b128 v[172:175], v208 offset:1600
	s_waitcnt lgkmcnt(5)
	v_mfma_f32_32x32x16_f16 v[34:49], v[146:149], v[176:179], v[34:49]
	ds_read_b128 v[176:179], v208 offset:1632
	s_waitcnt lgkmcnt(5)
	v_mfma_f32_32x32x16_f16 v[34:49], v[142:145], v[180:183], v[34:49]
	ds_read_b128 v[180:183], v208 offset:1680
	s_waitcnt lgkmcnt(5)
	v_mfma_f32_32x32x16_f16 v[34:49], v[138:141], v[184:187], v[34:49]
	ds_read_b128 v[184:187], v208 offset:1712
	s_waitcnt lgkmcnt(5)
	v_mfma_f32_32x32x16_f16 v[34:49], v[134:137], v[188:191], v[34:49]
	ds_read_b128 v[188:191], v208 offset:1760
	s_add_i32 s27, s12, -1
	s_add_i32 s28, s13, -1
	v_and_b32_e32 v196, 32, v0
	s_waitcnt lgkmcnt(5)
	v_mfma_f32_32x32x16_f16 v[34:49], v[130:133], v[192:195], v[34:49]
	ds_read_b128 v[192:195], v208 offset:1792
	s_movk_i32 s29, 0x50
	v_add_u32_e32 v168, s27, v168
	v_add_u32_e32 v169, s28, v169
	s_waitcnt lgkmcnt(5)
	v_mfma_f32_32x32x16_f16 v[34:49], v[126:129], v[172:175], v[34:49]
	ds_read_b128 v[172:175], v208 offset:3200
	v_max_u32_e32 v168, v168, v169
	v_cvt_pk_f16_f32 v18, v18, v19
	v_cvt_pk_f16_f32 v19, v26, v27
	s_waitcnt lgkmcnt(5)
	v_mfma_f32_32x32x16_f16 v[34:49], v[122:125], v[176:179], v[34:49]
	ds_read_b128 v[176:179], v208 offset:3232
	v_mad_u32_u24 v169, v166, s29, v196
	v_cmp_gt_u32_e64 s[30:31], 64, v168
	v_pk_max_f16 v19, v19, 0
	s_waitcnt lgkmcnt(5)
	v_mfma_f32_32x32x16_f16 v[34:49], v[118:121], v[180:183], v[34:49]
	ds_read_b128 v[180:183], v208 offset:3280
	v_pk_max_f16 v18, v18, 0
	v_cndmask_b32_e64 v26, 0, v19, s[30:31]
	v_cvt_pk_f16_f32 v19, v20, v21
	s_waitcnt lgkmcnt(5)
	v_mfma_f32_32x32x16_f16 v[34:49], v[114:117], v[184:187], v[34:49]
	ds_read_b128 v[184:187], v208 offset:3312
	v_cvt_pk_f16_f32 v20, v28, v29
	v_cvt_pk_f16_f32 v21, v30, v31
	v_pk_max_f16 v20, v20, 0
	s_waitcnt lgkmcnt(5)
	v_mfma_f32_32x32x16_f16 v[34:49], v[110:113], v[188:191], v[34:49]
	ds_read_b128 v[188:191], v208 offset:3360
	v_pk_max_f16 v21, v21, 0
	v_cndmask_b32_e64 v27, 0, v20, s[30:31]
	v_cvt_pk_f16_f32 v20, v22, v23
	s_waitcnt lgkmcnt(5)
	v_mfma_f32_32x32x16_f16 v[34:49], v[106:109], v[192:195], v[34:49]
	ds_read_b128 v[192:195], v208 offset:3392
	v_cndmask_b32_e64 v28, 0, v21, s[30:31]
	v_cvt_pk_f16_f32 v21, v24, v25
	v_pk_max_f16 v19, v19, 0
	s_waitcnt lgkmcnt(5)
	v_mfma_f32_32x32x16_f16 v[34:49], v[102:105], v[172:175], v[34:49]
	v_pk_max_f16 v20, v20, 0
	v_pk_max_f16 v21, v21, 0
	v_cvt_pk_f16_f32 v22, v32, v33
	s_waitcnt lgkmcnt(4)
	v_mfma_f32_32x32x16_f16 v[34:49], v[98:101], v[176:179], v[34:49]
	v_cndmask_b32_e64 v18, 0, v18, s[30:31]
	v_cndmask_b32_e64 v19, 0, v19, s[30:31]
	v_cndmask_b32_e64 v20, 0, v20, s[30:31]
	s_waitcnt lgkmcnt(3)
	v_mfma_f32_32x32x16_f16 v[34:49], v[94:97], v[180:183], v[34:49]
	v_cndmask_b32_e64 v21, 0, v21, s[30:31]
	v_pk_max_f16 v22, v22, 0
	s_nop 0
	s_waitcnt lgkmcnt(2)
	v_mfma_f32_32x32x16_f16 v[34:49], v[90:93], v[184:187], v[34:49]
	v_cndmask_b32_e64 v29, 0, v22, s[30:31]
	ds_write_b128 v169, v[18:21] offset:32000
	ds_write_b128 v169, v[26:29] offset:32016
	s_waitcnt lgkmcnt(3)
	v_mfma_f32_32x32x16_f16 v[34:49], v[86:89], v[188:191], v[34:49]
	s_waitcnt lgkmcnt(2)
	v_mfma_f32_32x32x16_f16 v[34:49], v[82:85], v[192:195], v[34:49]
	s_or_b64 exec, exec, s[2:3]
	s_add_i32 s12, s12, -1
	s_add_i32 s13, s13, -1
	v_and_b32_e32 v171, 32, v0
	s_branch .LBB1_6
